# grid barrier leader tail: unused per-XCD generation add and its two vmcnt(0) waits dropped
# speedup vs baseline: 1.0119x; 1.0115x over previous
.LBB0_269:
	s_or_b64 exec, exec, s[6:7]
	s_mov_b64 s[6:7], exec
	v_mbcnt_lo_u32_b32 v1, s6, 0
	v_mbcnt_hi_u32_b32 v1, s7, v1
	v_cmp_eq_u32_e32 vcc, 0, v1
	buffer_inv sc1
	s_and_saveexec_b64 s[8:9], vcc
	s_cbranch_execz .LBB0_271
	s_bcnt1_i32_b64 s2, s[6:7]
	v_mov_b32_e32 v1, 0x2000
	v_mov_b32_e32 v2, s2
.LBB0_271:
	s_or_b64 exec, exec, s[8:9]
.LBB0_272:
	s_or_b64 exec, exec, s[0:1]
	s_and_b32 s0, s43, 63
	s_cmp_eq_u32 s0, 0
	s_cselect_b64 s[30:31], -1, 0
	s_cmp_lg_u32 s0, 0
	s_cselect_b64 s[0:1], -1, 0
	s_and_b32 s89, s96, 63
	s_and_b64 vcc, exec, s[0:1]
	s_waitcnt lgkmcnt(0)
	s_barrier
	s_cbranch_vccz .LBB0_274
	s_mov_b64 s[4:5], -1
	s_mov_b64 s[34:35], 0
	s_mov_b32 s57, s43
	s_branch .LBB0_277

.LBB0_739:
	s_or_b64 exec, exec, s[8:9]
.LBB0_740:
	s_or_b64 exec, exec, s[0:1]
	s_add_u32 s4, s84, 0x39400000
	s_addc_u32 s5, s85, 0
	s_add_u32 s89, s84, 0xc000000
	s_addc_u32 s0, s85, 0
	v_writelane_b32 v251, s0, 2
	s_lshl_b32 s0, s43, 4
	v_writelane_b32 v251, s0, 3
	s_lshl_b32 s31, s96, 4
	s_mov_b32 s24, 0
	v_writelane_b32 v251, s1, 4
	s_mov_b32 s25, 0x7ffe0
	s_mov_b32 s26, 0x81020409
	s_mov_b32 s27, 0xfff81
	v_mov_b32_e32 v131, 0
	s_mov_b32 s28, 0x12000
	s_mov_b32 s29, 0x14000
	s_mov_b32 s30, 0x16000
	s_add_i32 s86, 0, 0x18000
	s_mov_b64 s[0:1], 0x80
	s_add_i32 s87, 0, 0x1c000
	s_mov_b64 s[6:7], 0x100
	s_mov_b64 s[8:9], 0x180
	s_mov_b64 s[10:11], 0x10000
	s_mov_b64 s[12:13], 0x12000
	s_mov_b64 s[14:15], 0x14000
	s_mov_b64 s[16:17], 0x16000
	s_waitcnt lgkmcnt(0)
	v_mov_b32_e32 v1, 1
	s_add_i32 s2, 0, 0x14000
	s_add_i32 s3, 0, 0x10000
	s_barrier
	v_writelane_b32 v251, s31, 5
	s_branch .LBB0_743

.LBB0_815:
	s_or_b64 exec, exec, s[8:9]
	s_mov_b64 s[8:9], exec
	v_mbcnt_lo_u32_b32 v1, s8, 0
	v_mbcnt_hi_u32_b32 v1, s9, v1
	v_cmp_eq_u32_e32 vcc, 0, v1
	buffer_inv sc1
	s_and_saveexec_b64 s[10:11], vcc
	s_cbranch_execz .LBB0_817
	s_bcnt1_i32_b64 s8, s[8:9]
	v_mov_b32_e32 v1, 0x2000
	v_mov_b32_e32 v2, s8
.LBB0_817:
	s_or_b64 exec, exec, s[10:11]
.LBB0_818:
	s_or_b64 exec, exec, s[0:1]
	s_add_u32 s0, s84, 0x3d400000
	s_addc_u32 s1, s85, 0
	v_mov_b32_e32 v22, v0
	v_writelane_b32 v251, s0, 6
	s_cmp_lt_i32 s96, 32
	s_movk_i32 s6, 0x80
	s_waitcnt lgkmcnt(0)
	s_barrier
	v_writelane_b32 v251, s1, 7
	s_cselect_b64 s[0:1], -1, 0
	v_cmp_gt_i32_e32 vcc, s6, v22
	s_and_b64 s[6:7], s[0:1], vcc
	s_and_saveexec_b64 s[0:1], s[6:7]
	s_cbranch_execz .LBB0_820
	s_ashr_i32 s97, s96, 31
	s_lshl_b64 s[6:7], s[96:97], 15
	v_readlane_b32 s8, v251, 6
	v_readlane_b32 s9, v251, 7
	s_add_u32 s6, s8, s6
	s_addc_u32 s7, s9, s7
	v_ashrrev_i32_e32 v23, 31, v22
	v_lshl_add_u64 v[2:3], v[22:23], 1, s[6:7]
	v_add_co_u32_e32 v2, vcc, 0x7000, v2
	v_mov_b32_e32 v1, 0
	s_nop 0
	v_addc_co_u32_e32 v3, vcc, 0, v3, vcc
	global_store_short v[2:3], v1, off offset:3840

.LBB0_890:
	s_or_b64 exec, exec, s[10:11]
.LBB0_891:
	s_or_b64 exec, exec, s[0:1]
	s_waitcnt vmcnt(7)
	v_cndmask_b32_e64 v2, 0, 1, s[4:5]
	v_cmp_ne_u32_e64 s[0:1], 1, v2
	s_waitcnt lgkmcnt(0)
	v_mov_b32_e32 v1, v0
	s_andn2_b64 vcc, exec, s[4:5]
	v_writelane_b32 v251, s0, 8
	s_barrier
	s_nop 0
	v_writelane_b32 v251, s1, 9
	s_cbranch_vccnz .LBB0_931
	v_writelane_b32 v251, s89, 10
	v_writelane_b32 v251, s94, 11
	v_writelane_b32 v252, s92, 62
	s_mov_b32 s97, 0
	v_writelane_b32 v251, s95, 12
	v_writelane_b32 v252, s93, 63
	v_writelane_b32 v251, s90, 13
	v_readlane_b32 s0, v252, 0
	v_readlane_b32 s1, v252, 6
	v_writelane_b32 v251, s91, 14
	s_lshr_b32 s4, s0, 7
	s_lshl_b32 s0, s1, 5
	v_writelane_b32 v251, s88, 15
	s_and_b32 s0, s0, 32
	v_writelane_b32 v252, s0, 58
	v_writelane_b32 v251, s89, 16
	s_add_u32 s0, s84, 0x15000000
	v_writelane_b32 v251, s0, 17
	s_addc_u32 s0, s85, 0
	v_writelane_b32 v251, s0, 18
	s_mul_i32 s0, s1, 0x1200
	s_add_u32 s1, s84, 0x8000000
	v_writelane_b32 v251, s1, 19
	s_addc_u32 s1, s85, 0
	v_writelane_b32 v251, s1, 20
	s_add_u32 s1, s84, 0x1d400000
	v_writelane_b32 v251, s1, 21
	s_addc_u32 s1, s85, 0
	v_writelane_b32 v251, s1, 22
	s_add_i32 s92, s0, 0
	v_writelane_b32 v251, s4, 23
	s_lshl_b32 s0, s4, 11
	s_mov_b64 s[4:5], s[80:81]
	v_writelane_b32 v251, s0, 24
	s_mov_b64 s[6:7], s[82:83]
	s_mov_b64 s[8:9], s[84:85]
	v_writelane_b32 v251, s4, 25
	s_add_u32 s0, s84, 0x100000
	s_addc_u32 s1, s85, 0
	v_writelane_b32 v251, s5, 26
	v_writelane_b32 v251, s6, 27
	v_writelane_b32 v251, s7, 28
	v_writelane_b32 v251, s8, 29
	v_writelane_b32 v251, s9, 30
	v_writelane_b32 v251, s10, 31
	v_writelane_b32 v251, s11, 32
	v_writelane_b32 v251, s0, 33
	v_mov_b32_e32 v2, 0
	s_movk_i32 s82, 0x4000
	v_writelane_b32 v251, s1, 34
	s_mov_b32 s0, s96
	v_writelane_b32 v251, s0, 35
	v_mov_b32_e32 v194, 0xff800000
	s_mov_b32 s83, 0x41380000
	v_mov_b32_e32 v195, 0xf149f2ca
	s_add_i32 s85, 0, 0x12800
	v_mov_b32_e32 v196, 0x447a0000
	v_mov_b32_e32 v197, 0xc47a0000
	v_mbcnt_hi_u32_b32 v198, -1, v228
	v_writelane_b32 v251, s1, 36
	s_mov_b32 s1, s96
	v_readlane_b32 s100, v252, 41
	s_nop 3
	s_cmpk_lg_i32 s100, 0x100
	s_cbranch_scc1 .Lmy_nsa_nomap
	s_and_b32 s1, s96, 7
	s_lshl_b32 s1, s1, 1
	s_bfe_u32 s100, s96, 0x10003
	s_add_i32 s1, s1, s100
	s_lshl_b32 s1, s1, 4
	s_lshr_b32 s100, s96, 4
	s_add_i32 s1, s1, s100

.LBB0_983:
	s_or_b64 exec, exec, s[6:7]
	s_mov_b64 s[6:7], exec
	v_mbcnt_lo_u32_b32 v1, s6, 0
	v_mbcnt_hi_u32_b32 v1, s7, v1
	v_cmp_eq_u32_e32 vcc, 0, v1
	buffer_inv sc1
	s_and_saveexec_b64 s[8:9], vcc
	s_cbranch_execz .LBB0_985
	s_bcnt1_i32_b64 s6, s[6:7]
	v_mov_b32_e32 v1, 0x2000
	v_mov_b32_e32 v2, s6
.LBB0_985:
	s_or_b64 exec, exec, s[8:9]
.LBB0_986:
	s_or_b64 exec, exec, s[0:1]
	v_readlane_b32 s0, v252, 39
	v_mov_b32_e32 v13, v0
	v_readlane_b32 s1, v252, 40
	s_waitcnt lgkmcnt(0)
	s_barrier
	s_and_b64 vcc, exec, s[0:1]
	v_readfirstlane_b32 s8, v13
	s_cbranch_vccnz .LBB0_1017
	s_ashr_i32 s17, s96, 31
	s_lshr_b32 s0, s17, 29
	s_add_i32 s5, s96, s0
	s_and_b32 s0, s5, -8
	s_sub_i32 s6, s96, s0
	s_cmp_gt_i32 s6, -1
	s_cbranch_scc0 .LBB0_989
	s_lshl_b32 s4, s6, 6
	s_cbranch_execz .LBB0_990
	s_branch .LBB0_991

.LBB0_1068:
	s_or_b64 exec, exec, s[8:9]
.LBB0_1069:
	s_or_b64 exec, exec, s[0:1]
	s_add_u32 s33, s84, 0x29400000
	s_addc_u32 s34, s85, 0
	v_readlane_b32 s0, v252, 39
	s_add_u32 s35, s84, 0x3400000
	v_mov_b32_e32 v10, v0
	v_readlane_b32 s1, v252, 40
	s_waitcnt lgkmcnt(0)
	s_barrier
	s_addc_u32 s36, s85, 0
	s_and_b64 vcc, exec, s[0:1]
	v_readfirstlane_b32 s4, v10
	s_cbranch_vccnz .LBB0_1072
	s_ashr_i32 s0, s96, 31
	s_lshr_b32 s0, s0, 29
	s_add_i32 s7, s96, s0
	s_and_b32 s0, s7, -8
	s_sub_i32 s5, s96, s0
	s_cmp_gt_i32 s5, -1
	s_cbranch_scc0 .LBB0_1073
	s_lshl_b32 s6, s5, 6
	s_ashr_i32 s0, s7, 3
	s_cbranch_execz .LBB0_1074
	s_branch .LBB0_1075

.LBB0_1161:
	s_or_b64 exec, exec, s[10:11]
	s_mov_b64 s[10:11], exec
	v_mbcnt_lo_u32_b32 v1, s10, 0
	v_mbcnt_hi_u32_b32 v1, s11, v1
	v_cmp_eq_u32_e32 vcc, 0, v1
	buffer_inv sc1
	s_and_saveexec_b64 s[12:13], vcc
	s_cbranch_execz .LBB0_1163
	s_bcnt1_i32_b64 s10, s[10:11]
	v_mov_b32_e32 v1, 0x2000
	v_mov_b32_e32 v2, s10
.LBB0_1163:
	s_or_b64 exec, exec, s[12:13]
.LBB0_1164:
	s_or_b64 exec, exec, s[4:5]
	v_readlane_b32 s4, v251, 8
	s_add_u32 s18, s84, 0x45000000
	v_readlane_b32 s5, v251, 9
	v_mov_b32_e32 v2, v0
	s_addc_u32 s19, s85, 0
	s_and_b64 vcc, exec, s[4:5]
	s_waitcnt lgkmcnt(0)
	s_barrier
	s_cbranch_vccnz .LBB0_1266
	v_and_b32_e32 v6, 7, v2
	v_mbcnt_hi_u32_b32 v10, -1, v228
	v_lshlrev_b32_e32 v4, 4, v6
	v_mov_b32_e32 v5, 0
	v_and_b32_e32 v7, 64, v10
	v_lshl_add_u64 v[198:199], s[6:7], 0, v[4:5]
	v_xor_b32_e32 v4, 1, v10
	v_add_u32_e32 v11, 64, v7
	v_cmp_lt_i32_e32 vcc, v4, v11
	v_readlane_b32 s23, v252, 6
	s_add_i32 s8, 0, 0x10e00
	v_cndmask_b32_e32 v4, v10, v4, vcc
	v_lshlrev_b32_e32 v230, 2, v4
	v_xor_b32_e32 v4, 2, v10
	v_cmp_lt_i32_e32 vcc, v4, v11
	s_lshl_b32 s22, s23, 5
	v_and_b32_e32 v1, 15, v2
	v_cndmask_b32_e32 v4, v10, v4, vcc
	v_lshlrev_b32_e32 v231, 2, v4
	v_xor_b32_e32 v4, 4, v10
	v_bfe_u32 v3, v2, 3, 3
	v_cmp_lt_i32_e32 vcc, v4, v11
	s_add_i32 s6, s8, s22
	s_mov_b32 s21, 0
	v_cndmask_b32_e32 v4, v10, v4, vcc
	v_lshl_add_u32 v233, v3, 2, s6
	s_lshl_b32 s20, s23, 8
	s_lshl_b32 s6, s23, 9
	v_lshlrev_b32_e32 v8, 12, v1
	v_mov_b32_e32 v9, v5
	v_lshlrev_b32_e32 v232, 2, v4
	s_mov_b32 s7, s21
	s_add_u32 s0, s0, s6
	v_and_b32_e32 v4, 48, v2
	v_lshl_add_u64 v[8:9], s[84:85], 0, v[8:9]
	v_cmp_eq_u32_e64 s[4:5], 0, v6
	s_addc_u32 s1, s1, 0
	v_lshlrev_b32_e32 v6, 1, v4
	v_mov_b32_e32 v7, v5
	v_lshl_add_u64 v[8:9], v[8:9], 0, s[6:7]
	v_lshl_add_u64 v[200:201], s[0:1], 0, v[6:7]
	v_lshl_add_u64 v[6:7], v[8:9], 0, v[6:7]
	s_mov_b64 s[0:1], 0x210000
	v_lshl_add_u64 v[202:203], v[6:7], 0, s[0:1]
	s_mov_b64 s[0:1], 0x230000
	v_lshl_add_u64 v[204:205], v[6:7], 0, s[0:1]
	s_lshl_b64 s[0:1], s[20:21], 2
	s_add_u32 s0, s66, s0
	s_addc_u32 s1, s67, s1
	v_lshlrev_b32_e32 v8, 2, v4
	v_mov_b32_e32 v9, v5
	v_lshl_add_u64 v[206:207], s[0:1], 0, v[8:9]
	s_add_u32 s0, s84, s20
	s_addc_u32 s1, s85, 0
	v_lshl_or_b32 v229, s23, 3, v3
	v_lshl_add_u64 v[8:9], s[0:1], 0, v[4:5]
	s_mov_b64 s[0:1], 0x35400000
	v_lshlrev_b32_e32 v3, 2, v1
	v_lshl_add_u64 v[208:209], v[8:9], 0, s[0:1]
	v_add_u32_e32 v234, s8, v3
	s_mov_b64 s[0:1], 0x220000
	v_add_u32_e32 v8, 0, v3
	v_xor_b32_e32 v3, 16, v10
	v_lshl_add_u64 v[210:211], v[6:7], 0, s[0:1]
	s_mov_b64 s[0:1], 0x240000
	v_cmp_lt_i32_e32 vcc, v3, v11
	v_lshl_add_u64 v[212:213], v[6:7], 0, s[0:1]
	v_readlane_b32 s0, v252, 0
	v_cndmask_b32_e32 v3, v10, v3, vcc
	s_and_b32 s0, s0, 0x1ffffc0
	v_lshrrev_b32_e32 v4, 2, v2
	v_lshlrev_b32_e32 v236, 2, v3
	v_xor_b32_e32 v3, 8, v10
	v_and_or_b32 v4, v4, 12, s0
	v_cmp_lt_i32_e32 vcc, v3, v11
	s_movk_i32 s0, 0x100
	v_lshlrev_b32_e32 v6, 6, v2
	v_bfe_u32 v9, v2, 5, 1
	v_and_b32_e32 v235, 31, v2
	v_cndmask_b32_e32 v3, v10, v3, vcc
	v_cmp_gt_i32_e64 s[14:15], 32, v2
	v_cmp_gt_i32_e64 s[16:17], s0, v2
	v_lshlrev_b32_e32 v10, 2, v2
	s_add_i32 s0, 0, 0x10200
	v_ashrrev_i32_e32 v7, 31, v6
	v_ashrrev_i32_e32 v240, 2, v2
	v_lshlrev_b32_e32 v2, 4, v2
	v_lshlrev_b32_e32 v237, 2, v3
	v_add_u32_e32 v239, s0, v10
	v_lshl_add_u64 v[6:7], v[6:7], 2, s[84:85]
	s_mov_b64 s[0:1], 0x8000
	v_and_b32_e32 v2, 48, v2
	v_mov_b32_e32 v3, v5
	v_lshl_add_u64 v[216:217], v[6:7], 0, s[0:1]
	v_lshl_add_u64 v[2:3], s[84:85], 0, v[2:3]
	s_mov_b64 s[0:1], 0x45200000
	v_lshl_add_u64 v[218:219], v[2:3], 0, s[0:1]
	v_lshl_or_b32 v2, v9, 2, s22
	s_add_i32 s0, 0, 0x10600
	v_add_lshl_u32 v242, v2, v235, 2
	v_add_u32_e32 v243, 0x10e00, v2
	v_lshlrev_b32_e32 v2, 7, v9
	v_lshlrev_b32_e32 v12, 7, v4
	v_lshlrev_b32_e32 v4, 2, v235
	s_add_i32 s33, 0, 0x10a00
	v_add_u32_e32 v241, s0, v10
	v_lshl_or_b32 v2, s23, 10, v2
	s_movk_i32 s0, 0x200
	v_cmp_gt_u32_e64 s[6:7], 4, v235
	v_cmp_eq_u32_e64 s[8:9], 0, v235
	v_cmp_eq_u32_e64 s[10:11], 1, v235
	v_cmp_eq_u32_e64 s[12:13], 2, v235
	v_lshl_add_u64 v[214:215], s[70:71], 0, v[4:5]
	v_add_u32_e32 v238, s33, v10
	v_or3_b32 v244, v2, v4, s0
	v_mov_b32_e32 v245, 0x3727c5ac
	s_mov_b64 s[22:23], 0x10000
	s_mov_b32 s40, 0x10000
	s_mov_b64 s[24:25], 0x20000
	s_mov_b32 s41, 0x20000
	s_mov_b64 s[26:27], 0x30000
	s_mov_b32 s42, 0x30000
	s_mov_b64 s[28:29], 0x10080
	s_mov_b64 s[30:31], 0x20080
	s_mov_b64 s[34:35], 0x30080
	s_mov_b32 s43, 0x8000
	s_mov_b32 s44, 0x18000
	v_add_u32_e32 v246, v8, v12
	v_mov_b32_e32 v247, 1
	v_mov_b32_e32 v248, 0xff800000
	s_mov_b32 s45, s96
	v_readlane_b32 s100, v252, 41
	s_nop 3
	s_cmpk_lg_i32 s100, 0x100
	s_cbranch_scc1 .Lmy_p7_nomap
	s_and_b32 s45, s96, 7
	s_lshl_b32 s45, s45, 5
	s_lshr_b32 s100, s96, 3
	s_add_i32 s45, s45, s100

.LBB0_1317:
	s_or_b64 exec, exec, s[8:9]
.LBB0_1318:
	s_or_b64 exec, exec, s[0:1]
	s_waitcnt lgkmcnt(0)
	v_mov_b32_e32 v1, v0
	s_barrier
	s_nop 0
	v_cmp_gt_i32_e64 s[0:1], 32, v1
	s_and_saveexec_b64 s[4:5], s[0:1]
	s_cbranch_execz .LBB0_1320
	v_lshlrev_b32_e32 v2, 6, v1
	v_ashrrev_i32_e32 v3, 31, v2
	v_lshl_add_u64 v[2:3], v[2:3], 2, s[84:85]
	v_add_co_u32_e32 v2, vcc, 0x8000, v2
	s_nop 1
	v_addc_co_u32_e32 v3, vcc, 0, v3, vcc
	global_load_dword v2, v[2:3], off sc1
	v_lshl_add_u32 v3, v1, 2, 0
	v_add_u32_e32 v3, 0x20000, v3
	s_waitcnt vmcnt(0)
	ds_write_b32 v3, v2

.LBB0_1407:
	s_or_b64 exec, exec, s[10:11]
.LBB0_1408:
	s_or_b64 exec, exec, s[4:5]
	s_add_u32 s4, s84, 0x57800000
	s_addc_u32 s5, s85, 0
	s_add_i32 s6, 0, 0x20100
	v_mov_b32_e32 v11, v0
	s_waitcnt lgkmcnt(0)
	v_mov_b32_e32 v1, s6
	s_barrier
	ds_read_b32 v1, v1
	s_ashr_i32 s24, s96, 3
	v_readfirstlane_b32 s10, v11
	s_waitcnt lgkmcnt(0)
	v_readfirstlane_b32 s6, v1
	s_cmp_ge_i32 s24, s6
	s_cbranch_scc1 .LBB0_1426
	v_lshlrev_b32_e32 v1, 4, v11
	v_add_u32_e32 v2, 0x2000, v1
	v_ashrrev_i32_e32 v3, 31, v2
	v_lshrrev_b32_e32 v3, 22, v3
	v_add_u32_e32 v3, v2, v3
	v_ashrrev_i32_e32 v10, 10, v3
	v_mul_i32_i24_e32 v3, 0x400, v10
	v_sub_u32_e32 v2, v2, v3
	v_lshrrev_b32_e32 v3, 4, v2
	v_bitop3_b32 v2, v3, v2, 32 bitop3:0x6c
	v_ashrrev_i32_e32 v3, 31, v2
	v_lshrrev_b32_e32 v3, 26, v3
	v_add_u32_e32 v3, v2, v3
	v_lshlrev_b32_e32 v4, 3, v10
	v_ashrrev_i32_e32 v12, 6, v3
	v_and_b32_e32 v4, -16, v4
	v_add_u32_e32 v4, v12, v4
	v_and_b32_e32 v5, 3, v12
	s_mov_b32 s6, 0x1fffe0
	v_lshrrev_b32_e32 v6, 2, v4
	v_lshlrev_b32_e32 v7, 1, v4
	v_and_b32_e32 v3, 0xc0, v3
	v_and_or_b32 v5, v4, s6, v5
	v_and_b32_e32 v6, 4, v6
	v_and_b32_e32 v7, 24, v7
	v_sub_u32_e32 v2, v2, v3
	v_mov_b32_e32 v3, 1
	v_or3_b32 v5, v5, v6, v7
	v_lshlrev_b32_e32 v6, 5, v10
	v_ashrrev_i16_sdwa v2, v3, sext(v2) dst_sel:DWORD dst_unused:UNUSED_PAD src0_sel:DWORD src1_sel:BYTE_0
	v_and_b32_e32 v6, 32, v6
	v_bfe_i32 v13, v2, 0, 16
	v_add_lshl_u32 v2, v6, v13, 1
	v_lshl_add_u32 v162, v5, 11, v2
	v_bfe_i32 v5, v11, 27, 1
	v_lshrrev_b32_e32 v5, 22, v5
	v_add_u32_e32 v5, v1, v5
	v_and_b32_e32 v5, 0xfffffc00, v5
	v_sub_u32_e32 v1, v1, v5
	v_lshrrev_b32_e32 v5, 4, v1
	v_ashrrev_i32_e32 v6, 31, v11
	v_bitop3_b32 v1, v5, v1, 32 bitop3:0x6c
	v_lshrrev_b32_e32 v6, 26, v6
	v_ashrrev_i32_e32 v5, 31, v1
	v_add_u32_e32 v6, v11, v6
	v_lshrrev_b32_e32 v5, 26, v5
	v_ashrrev_i32_e32 v15, 6, v6
	v_add_u32_e32 v5, v1, v5
	v_lshlrev_b32_e32 v6, 3, v15
	v_ashrrev_i32_e32 v14, 6, v5
	v_and_b32_e32 v6, -16, v6
	s_add_u32 s33, s84, 0x89800000
	v_add_u32_e32 v6, v14, v6
	v_and_b32_e32 v7, 3, v14
	s_addc_u32 s36, s85, 0
	v_and_or_b32 v7, v6, s6, v7
	s_lshl_b32 s6, s24, 2
	v_and_b32_e32 v5, 0xc0, v5
	s_add_i32 s6, s6, 0
	v_sub_u32_e32 v1, v1, v5
	s_add_i32 s6, s6, 0x20120
	v_ashrrev_i16_sdwa v1, v3, sext(v1) dst_sel:DWORD dst_unused:UNUSED_PAD src0_sel:DWORD src1_sel:BYTE_0
	v_mov_b32_e32 v3, s6
	ds_read_b32 v3, v3
	s_ashr_i32 s8, s10, 6
	s_ashr_i32 s25, s24, 31
	s_ashr_i32 s11, s10, 8
	s_lshl_b32 s37, s8, 10
	s_and_b32 s49, s96, 7
	s_lshl_b64 s[6:7], s[24:25], 19
	s_waitcnt lgkmcnt(0)
	v_readfirstlane_b32 s28, v3
	s_add_u32 s26, s0, s6
	s_addc_u32 s27, s1, s7
	s_ashr_i32 s29, s28, 31
	v_lshrrev_b32_e32 v8, 2, v6
	v_lshlrev_b32_e32 v9, 1, v6
	s_lshl_b32 s9, s49, 19
	s_lshl_b64 s[6:7], s[28:29], 22
	v_and_b32_e32 v8, 4, v8
	v_and_b32_e32 v9, 24, v9
	s_add_u32 s6, s33, s6
	v_or3_b32 v7, v7, v8, v9
	v_lshlrev_b32_e32 v8, 5, v15
	s_addc_u32 s7, s36, s7
	v_and_b32_e32 v8, 32, v8
	v_bfe_i32 v16, v1, 0, 16
	s_add_u32 s30, s6, s9
	v_add_lshl_u32 v1, v8, v16, 1
	s_addc_u32 s31, s7, 0
	s_add_i32 s38, s37, 0
	v_lshl_add_u32 v164, v7, 11, v1
	s_add_i32 m0, s38, 0x10000
	v_lshl_add_u32 v166, v6, 11, v1
	global_load_lds_dwordx4 v164, s[30:31]
	s_add_i32 m0, s38, 0x12000
	s_add_u32 s6, s30, 0x40000
	global_load_lds_dwordx4 v162, s[30:31]
	s_addc_u32 s7, s31, 0
	s_add_i32 m0, s38, 0x14000
	s_add_i32 s39, s38, 0x2000
	global_load_lds_dwordx4 v164, s[6:7]
	s_add_i32 m0, s38, 0x16000
	v_lshl_add_u32 v168, v4, 11, v2
	global_load_lds_dwordx4 v162, s[6:7]
	s_mov_b32 m0, s38
	s_add_i32 s40, s38, 0x4000
	global_load_lds_dwordx4 v166, s[26:27]
	s_mov_b32 m0, s39
	v_add_u32_e32 v170, 0x40000, v166
	global_load_lds_dwordx4 v168, s[26:27]
	s_mov_b32 m0, s40
	s_add_i32 s41, s38, 0x6000
	v_add_u32_e32 v172, 0x40000, v168
	global_load_lds_dwordx4 v170, s[26:27]
	s_mov_b32 m0, s41
	v_mov_b32_e32 v165, 0
	global_load_lds_dwordx4 v172, s[26:27]
	v_mov_b32_e32 v163, v165
	v_mov_b32_e32 v167, v165
	v_mov_b32_e32 v169, v165
	s_cmp_eq_u32 s11, 1
	s_mov_b32 s42, 0x40000
	v_lshl_add_u64 v[8:9], s[30:31], 0, v[164:165]
	v_lshl_add_u64 v[6:7], s[30:31], 0, v[162:163]
	v_lshl_add_u64 v[2:3], s[26:27], 0, v[166:167]
	s_cselect_b64 s[6:7], -1, 0
	s_cmp_lg_u32 s11, 1
	v_lshl_add_u64 v[4:5], s[26:27], 0, v[168:169]
	s_cbranch_scc1 .LBB0_1411
	s_barrier

.LBB0_1477:
	s_or_b64 exec, exec, s[8:9]
.LBB0_1478:
	s_or_b64 exec, exec, s[0:1]
	s_andn2_b64 vcc, exec, s[92:93]
	s_waitcnt lgkmcnt(0)
	s_barrier
	s_cbranch_vccnz .LBB0_1481
	v_and_b32_e32 v1, 63, v0
	v_lshlrev_b32_e32 v2, 2, v0
	v_lshlrev_b32_e32 v16, 3, v1
	v_lshrrev_b32_e32 v0, 2, v0
	v_and_b32_e32 v2, 4, v2
	v_and_b32_e32 v3, 0xf0, v16
	v_and_b32_e32 v0, 8, v0
	v_or3_b32 v4, v3, v0, v2
	v_mbcnt_hi_u32_b32 v0, -1, v228
	v_and_b32_e32 v2, 64, v0
	v_add_u32_e32 v2, 64, v2
	v_xor_b32_e32 v3, 32, v0
	v_cmp_lt_i32_e32 vcc, v3, v2
	s_ashr_i32 s91, s90, 31
	s_ashr_i32 s89, s88, 31
	v_cndmask_b32_e32 v3, v0, v3, vcc
	v_lshlrev_b32_e32 v22, 2, v3
	v_xor_b32_e32 v3, 16, v0
	v_cmp_lt_i32_e32 vcc, v3, v2
	s_lshl_b64 s[6:7], s[90:91], 12
	s_lshl_b64 s[0:1], s[90:91], 6
	v_cndmask_b32_e32 v3, v0, v3, vcc
	v_lshlrev_b32_e32 v23, 2, v3
	v_xor_b32_e32 v3, 8, v0
	v_cmp_lt_i32_e32 vcc, v3, v2
	s_lshl_b64 s[2:3], s[88:89], 6
	v_or_b32_e32 v16, s6, v16
	v_cndmask_b32_e32 v3, v0, v3, vcc
	v_lshlrev_b32_e32 v24, 2, v3
	v_xor_b32_e32 v3, 4, v0
	v_cmp_lt_i32_e32 vcc, v3, v2
	v_mov_b32_e32 v17, s7
	s_lshl_b64 s[6:7], s[88:89], 12
	v_cndmask_b32_e32 v3, v0, v3, vcc
	v_lshlrev_b32_e32 v25, 2, v3
	v_xor_b32_e32 v3, 2, v0
	v_cmp_lt_i32_e32 vcc, v3, v2
	s_lshl_b64 s[8:9], s[90:91], 13
	s_add_u32 s8, s82, s8
	v_cndmask_b32_e32 v3, v0, v3, vcc
	v_lshlrev_b32_e32 v26, 2, v3
	v_xor_b32_e32 v3, 1, v0
	v_cmp_lt_i32_e32 vcc, v3, v2
	s_addc_u32 s9, s83, s9
	v_mov_b32_e32 v28, 0x45200000
	v_cndmask_b32_e32 v0, v0, v3, vcc
	v_lshlrev_b32_e32 v27, 2, v0
	v_lshlrev_b32_e32 v0, 4, v1
	v_mov_b32_e32 v1, 0
	v_or_b32_e32 v2, 0x1000, v0
	v_mov_b32_e32 v3, v1
	v_lshl_add_u64 v[8:9], s[80:81], 0, v[2:3]
	v_or_b32_e32 v2, 0x1400, v0
	v_lshl_add_u64 v[10:11], s[80:81], 0, v[2:3]
	v_or_b32_e32 v2, 0x1800, v0
	v_lshl_add_u64 v[6:7], s[80:81], 0, v[0:1]
	v_mov_b32_e32 v5, v1
	v_lshl_add_u64 v[12:13], s[80:81], 0, v[2:3]
	v_or_b32_e32 v2, 0x1c00, v0
	v_lshl_add_u64 v[0:1], s[8:9], 0, v[0:1]
	s_mov_b64 s[8:9], 0x1000
	v_lshl_add_u64 v[14:15], s[80:81], 0, v[2:3]
	v_lshl_add_u64 v[18:19], v[0:1], 0, s[8:9]
	s_lshl_b64 s[8:9], s[88:89], 13
	s_add_i32 s12, 0, 0x20080
	v_mov_b32_e32 v29, 0x3727c5ac
	global_load_dwordx4 v[196:199], v[6:7], off
	global_load_dwordx4 v[200:203], v[6:7], off offset:1024
	global_load_dwordx4 v[204:207], v[6:7], off offset:2048
	global_load_dwordx4 v[208:211], v[6:7], off offset:3072
	global_load_dwordx4 v[212:215], v[8:9], off
	global_load_dwordx4 v[216:219], v[10:11], off
	global_load_dwordx4 v[220:223], v[12:13], off
	global_load_dwordx4 v[224:227], v[14:15], off
